# baseline (speedup 1.0000x reference)
.LBB0_16:
	global_load_dwordx4 v[6:9], v[2:3], off offset:-16
	global_load_dwordx4 v[10:13], v[2:3], off
	s_nop 0
	v_lshl_add_u64 v[2:3], v[2:3], 0, s[2:3]
	global_load_dwordx4 v[22:25], v[2:3], off offset:-16
	global_load_dwordx4 v[26:29], v[2:3], off
	s_nop 0
	v_lshl_add_u64 v[2:3], v[2:3], 0, s[2:3]
	v_and_b32_e32 v15, 8, v1
	v_and_b32_e32 v14, 0x3ff, v0
	v_add_u32_e32 v16, 0x100, v0
	v_mul_u32_u24_e32 v18, 0x408, v15
	v_add_u32_e32 v1, 2, v1
	v_add_u32_e32 v17, 0x1020, v14
	v_mad_u32_u24 v19, v15, s4, v4
	v_mad_u32_u24 v15, v15, s4, v5
	v_mov_b32_e32 v0, v16
	v_add_lshl_u32 v16, v18, v14, 1
	v_add_lshl_u32 v18, v17, v18, 1
	v_add_lshl_u32 v20, v19, v14, 1
	v_add_lshl_u32 v19, v17, v19, 1
	v_add_lshl_u32 v14, v15, v14, 1
	v_add_lshl_u32 v15, v17, v15, 1
	s_waitcnt vmcnt(2)
	v_cvt_f16_f32_e32 v6, v6
	v_cvt_f16_f32_e32 v10, v10
	v_cvt_f16_f32_e32 v7, v7
	v_cvt_f16_f32_e32 v11, v11
	v_cvt_f16_f32_e32 v8, v8
	v_cvt_f16_f32_e32 v12, v12
	v_cvt_f16_f32_e32 v9, v9
	v_cvt_f16_f32_e32 v13, v13
	global_store_short v16, v6, s[22:23]
	global_store_short v18, v10, s[22:23]
	global_store_short v16, v7, s[22:23] offset:2064
	global_store_short v18, v11, s[22:23] offset:2064
	global_store_short v20, v8, s[22:23]
	global_store_short v19, v12, s[22:23]
	global_store_short v14, v9, s[22:23]
	global_store_short v15, v13, s[22:23]
	global_load_dwordx4 v[6:9], v[2:3], off offset:-16
	global_load_dwordx4 v[10:13], v[2:3], off
	s_nop 0
	v_lshl_add_u64 v[2:3], v[2:3], 0, s[2:3]
	v_and_b32_e32 v15, 8, v1
	v_and_b32_e32 v14, 0x3ff, v0
	v_add_u32_e32 v16, 0x100, v0
	v_mul_u32_u24_e32 v18, 0x408, v15
	v_add_u32_e32 v1, 2, v1
	v_add_u32_e32 v17, 0x1020, v14
	v_mad_u32_u24 v19, v15, s4, v4
	v_mad_u32_u24 v15, v15, s4, v5
	v_mov_b32_e32 v0, v16
	v_add_lshl_u32 v16, v18, v14, 1
	v_add_lshl_u32 v18, v17, v18, 1
	v_add_lshl_u32 v20, v19, v14, 1
	v_add_lshl_u32 v19, v17, v19, 1
	v_add_lshl_u32 v14, v15, v14, 1
	v_add_lshl_u32 v15, v17, v15, 1
	s_waitcnt vmcnt(10)
	v_cvt_f16_f32_e32 v22, v22
	v_cvt_f16_f32_e32 v26, v26
	v_cvt_f16_f32_e32 v23, v23
	v_cvt_f16_f32_e32 v27, v27
	v_cvt_f16_f32_e32 v24, v24
	v_cvt_f16_f32_e32 v28, v28
	v_cvt_f16_f32_e32 v25, v25
	v_cvt_f16_f32_e32 v29, v29
	global_store_short v16, v22, s[22:23]
	global_store_short v18, v26, s[22:23]
	global_store_short v16, v23, s[22:23] offset:2064
	global_store_short v18, v27, s[22:23] offset:2064
	global_store_short v20, v24, s[22:23]
	global_store_short v19, v28, s[22:23]
	global_store_short v14, v25, s[22:23]
	global_store_short v15, v29, s[22:23]
	global_load_dwordx4 v[22:25], v[2:3], off offset:-16
	global_load_dwordx4 v[26:29], v[2:3], off
	s_nop 0
	v_lshl_add_u64 v[2:3], v[2:3], 0, s[2:3]
	v_and_b32_e32 v15, 8, v1
	v_and_b32_e32 v14, 0x3ff, v0
	v_add_u32_e32 v16, 0x100, v0
	v_mul_u32_u24_e32 v18, 0x408, v15
	v_add_u32_e32 v1, 2, v1
	v_add_u32_e32 v17, 0x1020, v14
	v_mad_u32_u24 v19, v15, s4, v4
	v_mad_u32_u24 v15, v15, s4, v5
	v_mov_b32_e32 v0, v16
	v_add_lshl_u32 v16, v18, v14, 1
	v_add_lshl_u32 v18, v17, v18, 1
	v_add_lshl_u32 v20, v19, v14, 1
	v_add_lshl_u32 v19, v17, v19, 1
	v_add_lshl_u32 v14, v15, v14, 1
	v_add_lshl_u32 v15, v17, v15, 1
	s_waitcnt vmcnt(10)
	v_cvt_f16_f32_e32 v6, v6
	v_cvt_f16_f32_e32 v10, v10
	v_cvt_f16_f32_e32 v7, v7
	v_cvt_f16_f32_e32 v11, v11
	v_cvt_f16_f32_e32 v8, v8
	v_cvt_f16_f32_e32 v12, v12
	v_cvt_f16_f32_e32 v9, v9
	v_cvt_f16_f32_e32 v13, v13
	global_store_short v16, v6, s[22:23]
	global_store_short v18, v10, s[22:23]
	global_store_short v16, v7, s[22:23] offset:2064
	global_store_short v18, v11, s[22:23] offset:2064
	global_store_short v20, v8, s[22:23]
	global_store_short v19, v12, s[22:23]
	global_store_short v14, v9, s[22:23]
	global_store_short v15, v13, s[22:23]
	global_load_dwordx4 v[6:9], v[2:3], off offset:-16
	global_load_dwordx4 v[10:13], v[2:3], off
	s_nop 0
	v_lshl_add_u64 v[2:3], v[2:3], 0, s[2:3]
	v_and_b32_e32 v15, 8, v1
	v_and_b32_e32 v14, 0x3ff, v0
	v_add_u32_e32 v16, 0x100, v0
	v_mul_u32_u24_e32 v18, 0x408, v15
	v_add_u32_e32 v1, 2, v1
	v_add_u32_e32 v17, 0x1020, v14
	v_mad_u32_u24 v19, v15, s4, v4
	v_mad_u32_u24 v15, v15, s4, v5
	v_mov_b32_e32 v0, v16
	v_add_lshl_u32 v16, v18, v14, 1
	v_add_lshl_u32 v18, v17, v18, 1
	v_add_lshl_u32 v20, v19, v14, 1
	v_add_lshl_u32 v19, v17, v19, 1
	v_add_lshl_u32 v14, v15, v14, 1
	v_add_lshl_u32 v15, v17, v15, 1
	s_waitcnt vmcnt(10)
	v_cvt_f16_f32_e32 v22, v22
	v_cvt_f16_f32_e32 v26, v26
	v_cvt_f16_f32_e32 v23, v23
	v_cvt_f16_f32_e32 v27, v27
	v_cvt_f16_f32_e32 v24, v24
	v_cvt_f16_f32_e32 v28, v28
	v_cvt_f16_f32_e32 v25, v25
	v_cvt_f16_f32_e32 v29, v29
	global_store_short v16, v22, s[22:23]
	global_store_short v18, v26, s[22:23]
	global_store_short v16, v23, s[22:23] offset:2064
	global_store_short v18, v27, s[22:23] offset:2064
	global_store_short v20, v24, s[22:23]
	global_store_short v19, v28, s[22:23]
	global_store_short v14, v25, s[22:23]
	global_store_short v15, v29, s[22:23]
	global_load_dwordx4 v[22:25], v[2:3], off offset:-16
	global_load_dwordx4 v[26:29], v[2:3], off
	s_nop 0
	v_lshl_add_u64 v[2:3], v[2:3], 0, s[2:3]
	v_and_b32_e32 v15, 8, v1
	v_and_b32_e32 v14, 0x3ff, v0
	v_add_u32_e32 v16, 0x100, v0
	v_mul_u32_u24_e32 v18, 0x408, v15
	v_add_u32_e32 v1, 2, v1
	v_add_u32_e32 v17, 0x1020, v14
	v_mad_u32_u24 v19, v15, s4, v4
	v_mad_u32_u24 v15, v15, s4, v5
	v_mov_b32_e32 v0, v16
	v_add_lshl_u32 v16, v18, v14, 1
	v_add_lshl_u32 v18, v17, v18, 1
	v_add_lshl_u32 v20, v19, v14, 1
	v_add_lshl_u32 v19, v17, v19, 1
	v_add_lshl_u32 v14, v15, v14, 1
	v_add_lshl_u32 v15, v17, v15, 1
	s_waitcnt vmcnt(10)
	v_cvt_f16_f32_e32 v6, v6
	v_cvt_f16_f32_e32 v10, v10
	v_cvt_f16_f32_e32 v7, v7
	v_cvt_f16_f32_e32 v11, v11
	v_cvt_f16_f32_e32 v8, v8
	v_cvt_f16_f32_e32 v12, v12
	v_cvt_f16_f32_e32 v9, v9
	v_cvt_f16_f32_e32 v13, v13
	global_store_short v16, v6, s[22:23]
	global_store_short v18, v10, s[22:23]
	global_store_short v16, v7, s[22:23] offset:2064
	global_store_short v18, v11, s[22:23] offset:2064
	global_store_short v20, v8, s[22:23]
	global_store_short v19, v12, s[22:23]
	global_store_short v14, v9, s[22:23]
	global_store_short v15, v13, s[22:23]
	global_load_dwordx4 v[6:9], v[2:3], off offset:-16
	global_load_dwordx4 v[10:13], v[2:3], off
	s_nop 0
	v_lshl_add_u64 v[2:3], v[2:3], 0, s[2:3]
	v_and_b32_e32 v15, 8, v1
	v_and_b32_e32 v14, 0x3ff, v0
	v_add_u32_e32 v16, 0x100, v0
	v_mul_u32_u24_e32 v18, 0x408, v15
	v_add_u32_e32 v1, 2, v1
	v_add_u32_e32 v17, 0x1020, v14
	v_mad_u32_u24 v19, v15, s4, v4
	v_mad_u32_u24 v15, v15, s4, v5
	v_mov_b32_e32 v0, v16
	v_add_lshl_u32 v16, v18, v14, 1
	v_add_lshl_u32 v18, v17, v18, 1
	v_add_lshl_u32 v20, v19, v14, 1
	v_add_lshl_u32 v19, v17, v19, 1
	v_add_lshl_u32 v14, v15, v14, 1
	v_add_lshl_u32 v15, v17, v15, 1
	s_waitcnt vmcnt(10)
	v_cvt_f16_f32_e32 v22, v22
	v_cvt_f16_f32_e32 v26, v26
	v_cvt_f16_f32_e32 v23, v23
	v_cvt_f16_f32_e32 v27, v27
	v_cvt_f16_f32_e32 v24, v24
	v_cvt_f16_f32_e32 v28, v28
	v_cvt_f16_f32_e32 v25, v25
	v_cvt_f16_f32_e32 v29, v29
	global_store_short v16, v22, s[22:23]
	global_store_short v18, v26, s[22:23]
	global_store_short v16, v23, s[22:23] offset:2064
	global_store_short v18, v27, s[22:23] offset:2064
	global_store_short v20, v24, s[22:23]
	global_store_short v19, v28, s[22:23]
	global_store_short v14, v25, s[22:23]
	global_store_short v15, v29, s[22:23]
	global_load_dwordx4 v[22:25], v[2:3], off offset:-16
	global_load_dwordx4 v[26:29], v[2:3], off
	s_nop 0
	v_lshl_add_u64 v[2:3], v[2:3], 0, s[2:3]
	v_and_b32_e32 v15, 8, v1
	v_and_b32_e32 v14, 0x3ff, v0
	v_add_u32_e32 v16, 0x100, v0
	v_mul_u32_u24_e32 v18, 0x408, v15
	v_add_u32_e32 v1, 2, v1
	v_add_u32_e32 v17, 0x1020, v14
	v_mad_u32_u24 v19, v15, s4, v4
	v_mad_u32_u24 v15, v15, s4, v5
	v_mov_b32_e32 v0, v16
	v_add_lshl_u32 v16, v18, v14, 1
	v_add_lshl_u32 v18, v17, v18, 1
	v_add_lshl_u32 v20, v19, v14, 1
	v_add_lshl_u32 v19, v17, v19, 1
	v_add_lshl_u32 v14, v15, v14, 1
	v_add_lshl_u32 v15, v17, v15, 1
	s_waitcnt vmcnt(10)
	v_cvt_f16_f32_e32 v6, v6
	v_cvt_f16_f32_e32 v10, v10
	v_cvt_f16_f32_e32 v7, v7
	v_cvt_f16_f32_e32 v11, v11
	v_cvt_f16_f32_e32 v8, v8
	v_cvt_f16_f32_e32 v12, v12
	v_cvt_f16_f32_e32 v9, v9
	v_cvt_f16_f32_e32 v13, v13
	global_store_short v16, v6, s[22:23]
	global_store_short v18, v10, s[22:23]
	global_store_short v16, v7, s[22:23] offset:2064
	global_store_short v18, v11, s[22:23] offset:2064
	global_store_short v20, v8, s[22:23]
	global_store_short v19, v12, s[22:23]
	global_store_short v14, v9, s[22:23]
	global_store_short v15, v13, s[22:23]
	v_and_b32_e32 v15, 8, v1
	v_and_b32_e32 v14, 0x3ff, v0
	v_add_u32_e32 v16, 0x100, v0
	v_mul_u32_u24_e32 v18, 0x408, v15
	v_add_u32_e32 v1, 2, v1
	v_add_u32_e32 v17, 0x1020, v14
	v_mad_u32_u24 v19, v15, s4, v4
	v_mad_u32_u24 v15, v15, s4, v5
	v_mov_b32_e32 v0, v16
	v_add_lshl_u32 v16, v18, v14, 1
	v_add_lshl_u32 v18, v17, v18, 1
	v_add_lshl_u32 v20, v19, v14, 1
	v_add_lshl_u32 v19, v17, v19, 1
	v_add_lshl_u32 v14, v15, v14, 1
	v_add_lshl_u32 v15, v17, v15, 1
	s_waitcnt vmcnt(8)
	v_cvt_f16_f32_e32 v22, v22
	v_cvt_f16_f32_e32 v26, v26
	v_cvt_f16_f32_e32 v23, v23
	v_cvt_f16_f32_e32 v27, v27
	v_cvt_f16_f32_e32 v24, v24
	v_cvt_f16_f32_e32 v28, v28
	v_cvt_f16_f32_e32 v25, v25
	v_cvt_f16_f32_e32 v29, v29
	global_store_short v16, v22, s[22:23]
	global_store_short v18, v26, s[22:23]
	global_store_short v16, v23, s[22:23] offset:2064
	global_store_short v18, v27, s[22:23] offset:2064
	global_store_short v20, v24, s[22:23]
	global_store_short v19, v28, s[22:23]
	global_store_short v14, v25, s[22:23]
	global_store_short v15, v29, s[22:23]
